# baseline (speedup 1.0000x reference)
.LBB2_2:
.LBB2_4:
	s_and_b64 s[2:3], s[2:3], exec
	s_cselect_b32 s10, s6, 0x752
	s_lshl_b32 s33, s10, 4
	s_add_i32 s2, s33, 0x7530
	v_or_b32_e32 v110, s2, v115
	v_mov_b32_e32 v111, 0
	s_waitcnt lgkmcnt(0)
	v_lshl_add_u64 v[2:3], v[110:111], 1, s[24:25]
	global_load_ushort v1, v[2:3], off
	s_mov_b64 s[4:5], 0x1d4c0
	v_lshl_add_u64 v[2:3], v[2:3], 0, s[4:5]
	global_load_ushort v199, v[2:3], off
	s_load_dwordx2 s[30:31], s[0:1], 0x20
	v_and_b32_e32 v110, 63, v0
	v_cmp_lt_u32_e32 vcc, 37, v110
	s_mul_hi_i32 s27, s10, 38
	s_mul_i32 s26, s10, 38
	s_waitcnt lgkmcnt(0)
	s_mul_i32 s86, s10, 0x980
	s_add_u32 s86, s30, s86
	s_addc_u32 s87, s31, 0
	v_and_b32_e32 v202, 60, v110
	global_load_dword v201, v202, s[86:87]
	global_load_dword v203, v202, s[86:87] offset:2432
	global_load_dword v120, v202, s[86:87] offset:64
	global_load_dword v200, v202, s[86:87] offset:2496
	global_load_dword v124, v202, s[86:87] offset:128
	global_load_dword v174, v202, s[86:87] offset:2560
	s_and_saveexec_b64 s[2:3], vcc
	s_xor_b64 s[2:3], exec, s[2:3]
	s_add_i32 s4, s10, 1
	s_ashr_i32 s5, s4, 31
	s_mul_hi_i32 s7, s4, 38
	s_mul_i32 s6, s4, 38
	s_or_saveexec_b64 s[2:3], s[2:3]
	s_load_dwordx2 s[34:35], s[0:1], 0x28
	v_mov_b64_e32 v[112:113], s[6:7]
	v_mov_b64_e32 v[2:3], s[4:5]
	s_xor_b64 exec, exec, s[2:3]
	s_cbranch_execz .LBB2_8
	v_mov_b32_e32 v111, 0
	v_lshl_add_u64 v[2:3], s[26:27], 0, v[110:111]
	v_lshlrev_b64 v[2:3], 6, v[2:3]
	s_waitcnt lgkmcnt(0)
	v_lshl_add_u64 v[18:19], s[30:31], 0, v[2:3]
	s_add_i32 s4, s10, 1
	global_load_dwordx4 v[2:5], v[18:19], off offset:16
	global_load_dwordx4 v[6:9], v[18:19], off
	global_load_dwordx4 v[10:13], v[18:19], off offset:48
	global_load_dwordx4 v[14:17], v[18:19], off offset:32
	v_mad_i64_i32 v[18:19], s[6:7], s4, 38, v[110:111]
	v_lshlrev_b64 v[18:19], 6, v[18:19]
	v_lshl_add_u64 v[34:35], s[30:31], 0, v[18:19]
	global_load_dwordx4 v[18:21], v[34:35], off
	global_load_dwordx4 v[22:25], v[34:35], off offset:16
	global_load_dwordx4 v[26:29], v[34:35], off offset:32
	global_load_dwordx4 v[30:33], v[34:35], off offset:48
	s_ashr_i32 s5, s4, 31
	s_mul_hi_i32 s7, s4, 38
	s_mul_i32 s6, s4, 38
	v_mov_b64_e32 v[112:113], s[6:7]
	s_waitcnt vmcnt(7)
	v_add_u32_e32 v2, v2, v3
	s_waitcnt vmcnt(6)
	v_add_u32_e32 v6, v6, v7
	v_add3_u32 v6, v6, v8, v9
	v_add3_u32 v2, v2, v4, v5
	s_waitcnt vmcnt(4)
	v_add_u32_e32 v3, v14, v15
	s_waitcnt vmcnt(3)
	v_sub_u32_e32 v5, v18, v6
	v_add_u32_e32 v5, v5, v19
	v_add3_u32 v5, v5, v20, v21
	v_sub_u32_e32 v2, v5, v2
	s_waitcnt vmcnt(2)
	v_add3_u32 v2, v2, v22, v23
	v_add3_u32 v3, v3, v16, v17
	v_add3_u32 v2, v2, v24, v25
	v_sub_u32_e32 v2, v2, v3
	v_add_u32_e32 v7, v10, v11
	s_waitcnt vmcnt(1)
	v_add3_u32 v2, v2, v26, v27
	v_add3_u32 v4, v7, v12, v13
	v_add3_u32 v2, v2, v28, v29
	v_sub_u32_e32 v2, v2, v4
	s_waitcnt vmcnt(0)
	v_add_u32_e32 v2, v2, v30
	v_add3_u32 v2, v2, v31, v32
	v_add3_u32 v2, v2, v33, 16
	v_min_i32_e32 v111, 0x300, v2
	v_mov_b64_e32 v[2:3], s[4:5]
.LBB2_8:
	s_or_b64 exec, exec, s[2:3]
	s_waitcnt vmcnt(0) lgkmcnt(0)
	v_cmp_lt_i32_e64 s[8:9], -1, v108
	s_and_saveexec_b64 s[88:89], s[8:9]
	s_cbranch_execz .Lmk_nxt_done
	v_mov_b32_e32 v109, 0
	v_lshl_add_u64 v[204:205], v[108:109], 2, s[20:21]
	global_load_dword v106, v[204:205], off
.Lmk_nxt_done:
	s_or_b64 exec, exec, s[88:89]
	s_lshl_b32 s39, s38, 11
	s_add_i32 s39, s39, 0x22000
	s_mul_hi_i32 s2, s10, 0x980
	s_mulk_i32 s10, 0x980
	s_movk_i32 s4, 0x980
	s_waitcnt lgkmcnt(0)
	s_add_u32 s36, s30, s10
	v_mov_b64_e32 v[8:9], s[30:31]
	s_addc_u32 s37, s31, s2
	v_mad_u64_u32 v[8:9], s[2:3], v2, s4, v[8:9]
	v_mov_b32_e32 v2, v9
	v_mad_u64_u32 v[2:3], s[2:3], v3, s4, v[2:3]
	v_mov_b32_e32 v5, 0
	v_and_b32_e32 v4, 60, v110
	v_mov_b32_e32 v9, v2
	v_lshl_add_u64 v[2:3], v[8:9], 0, v[4:5]
	v_mov_b32_e32 v6, v201
	v_mov_b32_e32 v11, v203
	v_and_b32_e32 v114, 3, v0
	v_cmp_eq_u32_e64 s[2:3], 0, v114
	s_mov_b32 s4, 0
	v_lshrrev_b32_e32 v34, 2, v110
	s_mov_b32 s6, s4
	s_mov_b32 s7, s4
	v_mul_u32_u24_e32 v7, 0x30d4, v34
	s_mov_b32 s5, s4
	v_mov_b32_e32 v117, v5
	v_mov_b64_e32 v[16:17], s[6:7]
	v_lshlrev_b32_e32 v116, 2, v7
	v_mov_b32_e32 v12, v5
	v_lshl_or_b32 v8, v110, 4, s39
	v_mov_b64_e32 v[14:15], s[4:5]
	v_lshl_add_u64 v[118:119], s[34:35], 0, v[116:117]
	v_lshlrev_b32_e32 v36, 2, v114
	ds_write_b128 v8, v[14:17]
	ds_write_b128 v8, v[14:17] offset:1024
	s_mul_i32 s84, s38, 0x2400
	v_lshl_add_u32 v206, v110, 4, s84
	ds_write_b128 v206, v[14:17]
	ds_write_b128 v206, v[14:17] offset:1024
	ds_write_b128 v206, v[14:17] offset:2048
	ds_write_b128 v206, v[14:17] offset:3072
	ds_write_b128 v206, v[14:17] offset:4096
	ds_write_b128 v206, v[14:17] offset:5120
	ds_write_b128 v206, v[14:17] offset:6144
	ds_write_b128 v206, v[14:17] offset:7168
	ds_write_b128 v206, v[14:17] offset:8192
	v_mov_b32_e32 v15, v5
	v_ashrrev_i32_e32 v7, 31, v6
	v_sub_u32_e32 v10, v11, v6
	v_cndmask_b32_e64 v13, 0, v10, s[2:3]
	v_lshl_add_u64 v[8:9], v[6:7], 2, v[118:119]
	v_cmp_lt_i32_e32 vcc, v114, v10
	v_add_u32_dpp v13, v13, v13 row_shr:1 row_mask:0xf bank_mask:0xf bound_ctrl:1
	s_nop 1
	v_add_u32_dpp v13, v13, v13 row_shr:2 row_mask:0xf bank_mask:0xf bound_ctrl:1
	s_nop 1
	v_add_u32_dpp v13, v13, v13 row_shr:4 row_mask:0xf bank_mask:0xf bound_ctrl:1
	s_nop 1
	v_add_u32_dpp v13, v13, v13 row_shr:8 row_mask:0xf bank_mask:0xf bound_ctrl:1
	s_nop 1
	v_add_u32_dpp v13, v13, v13 row_bcast:15 row_mask:0xa bank_mask:0xf
	s_nop 1
	v_mov_b32_dpp v12, v13 row_bcast:31 row_mask:0xc bank_mask:0xf
	s_and_saveexec_b64 s[4:5], vcc
	s_cbranch_execz .LBB2_10
	v_mov_b32_e32 v37, 0
	v_lshl_add_u64 v[14:15], v[8:9], 0, v[36:37]
	global_load_dword v15, v[14:15], off

.LBB2_31:
	s_or_b64 exec, exec, s[6:7]
	v_lshl_add_u64 v[4:5], s[36:37], 0, v[4:5]
	s_load_dwordx2 s[22:23], s[0:1], 0x38
	v_mov_b32_e32 v117, 0
	v_lshl_add_u64 v[6:7], s[34:35], 0, v[116:117]
	v_mov_b32_e32 v11, 0
	s_mov_b64 s[0:1], 0xc3500
	v_mov_b32_e32 v125, 0
	v_ashrrev_i32_e32 v121, 31, v120
	v_sub_u32_e32 v169, v200, v120
	v_cndmask_b32_e64 v12, 0, v169, s[2:3]
	v_lshl_add_u64 v[6:7], v[120:121], 2, v[6:7]
	v_cmp_lt_i32_e32 vcc, v114, v169
	v_add_u32_dpp v12, v12, v12 row_shr:1 row_mask:0xf bank_mask:0xf bound_ctrl:1
	v_lshl_add_u64 v[6:7], v[6:7], 0, s[0:1]
	s_nop 0
	v_add_u32_dpp v12, v12, v12 row_shr:2 row_mask:0xf bank_mask:0xf bound_ctrl:1
	s_nop 1
	v_add_u32_dpp v12, v12, v12 row_shr:4 row_mask:0xf bank_mask:0xf bound_ctrl:1
	s_nop 1
	v_add_u32_dpp v12, v12, v12 row_shr:8 row_mask:0xf bank_mask:0xf bound_ctrl:1
	s_nop 1
	v_add_u32_dpp v12, v12, v12 row_bcast:15 row_mask:0xa bank_mask:0xf
	s_nop 1
	v_mov_b32_dpp v11, v12 row_bcast:31 row_mask:0xc bank_mask:0xf
	s_and_saveexec_b64 s[0:1], vcc
	s_cbranch_execz .LBB2_33
	v_mov_b32_e32 v37, 0
	v_lshl_add_u64 v[14:15], v[6:7], 0, v[36:37]
	global_load_dword v125, v[14:15], off

.LBB2_47:
	s_or_b64 exec, exec, s[0:1]
	v_cmp_lt_i32_e32 vcc, v165, v169
	s_and_saveexec_b64 s[0:1], vcc
	s_cbranch_execz .LBB2_52
	v_add_u32_e32 v6, v12, v11
	v_add3_u32 v6, v6, v120, v114
	v_lshl_add_u32 v7, v6, 2, s40
	v_lshlrev_b32_e32 v8, 2, v200
	v_sub_u32_e32 v7, v7, v8
	v_sub_u32_e32 v6, v6, v200
	v_add_u32_e32 v8, 0xc80, v7
	v_add_u32_e32 v9, 32, v6
	v_mov_b32_e32 v7, 0
	v_mov_b32_e32 v6, v116
	v_lshl_add_u64 v[10:11], v[120:121], 2, v[6:7]
	v_mov_b32_e32 v37, v7
	v_lshl_add_u64 v[6:7], v[10:11], 0, v[36:37]
	v_lshl_add_u64 v[6:7], s[34:35], 0, v[6:7]
	s_mov_b64 s[6:7], 0xc3540
	v_lshl_add_u64 v[6:7], v[6:7], 0, s[6:7]
	s_mov_b64 s[6:7], 0
	v_mov_b32_e32 v10, v165
	s_branch .LBB2_50

.LBB2_52:
	s_or_b64 exec, exec, s[0:1]
	v_readlane_b32 s41, v111, 0
	v_lshrrev_b32_e32 v2, 1, v0
	v_and_b32_e32 v172, 28, v2
	v_cmp_gt_i32_e64 s[0:1], s41, v110
	v_or_b32_e32 v2, s40, v172
	v_lshlrev_b32_e32 v173, 2, v110
	v_mov_b32_e32 v4, 0
	s_mov_b64 vcc, s[0:1]
	v_or_b32_e32 v3, s40, v173
	ds_bpermute_b32 v9, v4, v4
	ds_read_b32 v5, v2 offset:0
	ds_read_b32 v6, v2 offset:32
	ds_read_b32 v7, v2 offset:64
	ds_read_b32 v8, v2 offset:96
	ds_read_b32 v40, v2 offset:128
	ds_read_b32 v39, v2 offset:160
	ds_read_b32 v38, v2 offset:192
	ds_read_b32 v37, v2 offset:224
	ds_read_b32 v121, v3
	s_waitcnt lgkmcnt(0)
	v_lshrrev_b32_e32 v175, 3, v110
	v_cmp_gt_i32_e32 vcc, s41, v175
	v_mov_b32_e32 v2, s33
	v_lshlrev_b32_e32 v122, 4, v110
	v_or_b32_e32 v177, 8, v175
	v_cndmask_b32_sdwa v3, v2, v5, vcc dst_sel:DWORD dst_unused:UNUSED_PAD src0_sel:DWORD src1_sel:WORD_0
	v_and_b32_e32 v176, 0x70, v122
	v_cmp_gt_i32_e32 vcc, s41, v177
	v_or_b32_e32 v178, 16, v175
	v_lshl_or_b32 v3, v3, 7, v176
	v_cndmask_b32_sdwa v4, v2, v6, vcc dst_sel:DWORD dst_unused:UNUSED_PAD src0_sel:DWORD src1_sel:WORD_0
	v_cmp_gt_i32_e32 vcc, s41, v178
	v_or_b32_e32 v179, 24, v175
	v_lshl_or_b32 v4, v4, 7, v176
	s_waitcnt lgkmcnt(0)
	global_load_dwordx4 v[10:13], v3, s[28:29]
	global_load_dwordx4 v[14:17], v4, s[28:29]
	v_cndmask_b32_sdwa v3, v2, v7, vcc dst_sel:DWORD dst_unused:UNUSED_PAD src0_sel:DWORD src1_sel:WORD_0
	v_cmp_gt_i32_e32 vcc, s41, v179
	v_lshl_or_b32 v3, v3, 7, v176
	s_mov_b32 s42, 0
	v_cndmask_b32_sdwa v2, v2, v8, vcc dst_sel:DWORD dst_unused:UNUSED_PAD src0_sel:DWORD src1_sel:WORD_0
	v_lshl_or_b32 v2, v2, 7, v176
	global_load_dwordx4 v[30:33], v3, s[28:29]
	global_load_dwordx4 v[26:29], v2, s[28:29]
	s_mov_b32 s43, 1
	s_cmp_lt_i32 s41, 33
	v_or_b32_e32 v180, 32, v175
	v_or_b32_e32 v181, 40, v175
	v_or_b32_e32 v182, 48, v175
	v_or_b32_e32 v183, 56, v175
	s_waitcnt vmcnt(3)
	v_mov_b64_e32 v[24:25], v[12:13]
	v_mov_b64_e32 v[20:21], v[12:13]
	v_mov_b64_e32 v[6:7], v[10:11]
	v_mov_b64_e32 v[2:3], v[10:11]
	v_mov_b64_e32 v[22:23], v[10:11]
	v_mov_b64_e32 v[18:19], v[10:11]
	v_mov_b64_e32 v[8:9], v[12:13]
	v_mov_b64_e32 v[4:5], v[12:13]
	s_cbranch_scc1 .LBB2_54
	v_cmp_gt_u32_e32 vcc, s41, v180
	v_mov_b32_e32 v18, s33
	s_nop 0
	v_cndmask_b32_sdwa v2, v18, v40, vcc dst_sel:DWORD dst_unused:UNUSED_PAD src0_sel:DWORD src1_sel:WORD_0
	v_cmp_gt_u32_e32 vcc, s41, v181
	v_lshl_or_b32 v19, v2, 7, v176
	s_nop 0
	v_cndmask_b32_sdwa v2, v18, v39, vcc dst_sel:DWORD dst_unused:UNUSED_PAD src0_sel:DWORD src1_sel:WORD_0
	v_cmp_gt_u32_e32 vcc, s41, v182
	v_lshl_or_b32 v20, v2, 7, v176
	global_load_dwordx4 v[2:5], v19, s[28:29]
	global_load_dwordx4 v[6:9], v20, s[28:29]
	v_cndmask_b32_sdwa v19, v18, v38, vcc dst_sel:DWORD dst_unused:UNUSED_PAD src0_sel:DWORD src1_sel:WORD_0
	v_cmp_gt_u32_e32 vcc, s41, v183
	v_lshl_or_b32 v38, v19, 7, v176
	s_nop 0
	v_cndmask_b32_sdwa v18, v18, v37, vcc dst_sel:DWORD dst_unused:UNUSED_PAD src0_sel:DWORD src1_sel:WORD_0
	v_lshl_or_b32 v37, v18, 7, v176
	global_load_dwordx4 v[18:21], v38, s[28:29]
	global_load_dwordx4 v[22:25], v37, s[28:29]

.LBB2_58:
	v_mov_b32_e32 v187, 0x4138aa3b
	v_lshrrev_b32_e32 v38, 3, v115
	v_lshlrev_b32_e32 v40, 5, v0
	v_lshrrev_b32_e32 v107, 4, v110
	s_lshl_b32 s6, s38, 13
	v_and_or_b32 v38, v175, 2, v38
	v_and_b32_e32 v40, 0x180, v40
	v_lshlrev_b32_e32 v41, 3, v0
	s_add_i32 s6, s6, 0x12000
	v_lshlrev_b32_e32 v39, 9, v107
	v_and_or_b32 v40, v41, 24, v40
	v_lshlrev_b32_e32 v38, 5, v38
	v_lshrrev_b32_e32 v37, 3, v0
	v_or3_b32 v39, v40, v39, s6
	v_xor_b32_e32 v40, 32, v38
	v_lshl_add_u32 v191, v110, 5, s39
	v_and_b32_e32 v0, 7, v0
	v_or_b32_e32 v186, v39, v38
	v_or_b32_e32 v188, v39, v40
	v_xor_b32_e32 v40, 64, v38
	v_xor_b32_e32 v38, 0x60, v38
	v_bitop3_b32 v0, v37, v0, 6 bitop3:0x6c
	v_or_b32_e32 v190, v39, v38
	v_and_b32_e32 v1, 0x380, v122
	v_lshlrev_b32_e32 v38, 4, v0
	v_add_u32_e32 v0, s33, v115
	v_or_b32_e32 v189, v39, v40
	v_lshlrev_b32_e32 v34, 2, v34
	v_mov_b32_e32 v35, 0
	v_and_b32_e32 v122, 6, v115
	v_xor_b32_e32 v122, v122, v107
	v_lshlrev_b32_e32 v122, 4, v122
	v_lshl_add_u32 v122, v115, 7, v122
	v_add_u32_e32 v122, s6, v122
	v_lshlrev_b32_e32 v206, 4, v107
	global_load_dwordx4 v[240:243], v206, s[58:59]
	global_load_dwordx4 v[244:247], v206, s[58:59] offset:64
	s_mov_b32 s60, 0xffff0000
	s_mov_b32 s61, 0
	s_mov_b32 s62, 0
	s_mov_b32 s63, 0xffff
	s_mov_b32 s64, 0
	s_mov_b32 s65, 0xffff0000
	v_or_b32_e32 v39, s6, v1
	v_add_u32_e32 v192, 0x15f90, v0
	v_lshlrev_b32_e32 v0, 7, v107
	v_and_b32_e32 v1, 0x78, v41
	v_lshl_add_u64 v[126:127], s[30:31], 0, v[34:35]
	v_or3_b32 v193, v1, v0, s39
	v_add_u32_e32 v0, s33, v110
	v_mov_b32_e32 v34, v116
	v_mov_b32_e32 v37, v35
	v_lshl_or_b32 v194, v110, 16, v0
	v_lshl_add_u64 v[0:1], v[34:35], 0, v[36:37]
	v_mov_b32_e32 v36, v35
	v_mov_b32_e32 v76, v35
	v_mov_b32_e32 v77, v35
	v_lshl_add_u64 v[0:1], s[34:35], 0, v[0:1]
	v_mov_b32_e32 v34, v35
	v_mov_b32_e32 v74, v35
	v_mov_b32_e32 v75, v35
	s_mov_b32 s12, 0x3c003c00
	v_mov_b64_e32 v[80:81], v[76:77]
	v_mov_b64_e32 v[84:85], v[76:77]
	v_mov_b64_e32 v[88:89], v[76:77]
	v_mov_b64_e32 v[92:93], v[76:77]
	v_mov_b64_e32 v[96:97], v[76:77]
	v_mov_b64_e32 v[100:101], v[76:77]
	v_mov_b64_e32 v[104:105], v[76:77]
	v_mov_b64_e32 v[56:57], v[36:37]
	v_mov_b64_e32 v[60:61], v[36:37]
	v_mov_b64_e32 v[64:65], v[36:37]
	v_mov_b64_e32 v[68:69], v[36:37]
	v_mov_b64_e32 v[72:73], v[36:37]
	s_or_b32 s47, s40, 0x80
	v_lshl_add_u64 v[0:1], v[0:1], 0, 64
	s_mov_b32 s49, 0
	s_mov_b64 s[30:31], -1
	s_mov_b32 s13, s12
	s_movk_i32 s48, 0x300
	v_mov_b32_e32 v116, 0xc3500
	v_lshlrev_b32_e32 v128, 2, v114
	v_add_u32_e32 v196, v39, v38
	v_mov_b64_e32 v[78:79], v[74:75]
	v_mov_b64_e32 v[82:83], v[74:75]
	v_mov_b64_e32 v[86:87], v[74:75]
	v_mov_b64_e32 v[90:91], v[74:75]
	v_mov_b64_e32 v[94:95], v[74:75]
	v_mov_b64_e32 v[98:99], v[74:75]
	v_mov_b64_e32 v[102:103], v[74:75]
	v_mov_b64_e32 v[54:55], v[34:35]
	v_mov_b64_e32 v[58:59], v[34:35]
	v_mov_b64_e32 v[62:63], v[34:35]
	v_mov_b64_e32 v[66:67], v[34:35]
	v_mov_b32_e32 v197, 0
	s_mov_b32 s50, 0
	v_mov_b64_e32 v[70:71], v[34:35]
	v_mov_b32_e32 v50, v35
	v_mov_b32_e32 v51, v35
	v_mov_b32_e32 v52, v35
	v_mov_b32_e32 v53, v35
	v_mov_b32_e32 v46, v35
	v_mov_b32_e32 v47, v35
	v_mov_b32_e32 v48, v35
	v_mov_b32_e32 v49, v35
	v_mov_b32_e32 v42, v35
	v_mov_b32_e32 v43, v35
	v_mov_b32_e32 v44, v35
	v_mov_b32_e32 v45, v35
	v_mov_b32_e32 v38, v35
	v_mov_b32_e32 v39, v35
	v_mov_b32_e32 v40, v35
	v_mov_b32_e32 v41, v35
	s_waitcnt vmcnt(0)
	ds_write_b128 v196, v[10:13]
	ds_write_b128 v196, v[14:17] offset:1024
	ds_write_b128 v196, v[30:33] offset:2048
	ds_write_b128 v196, v[26:29] offset:3072
	ds_write_b128 v196, v[2:5] offset:4096
	ds_write_b128 v196, v[6:9] offset:5120
	ds_write_b128 v196, v[18:21] offset:6144
	ds_write_b128 v196, v[22:25] offset:7168
	s_mul_i32 s78, s42, 0xc00
	s_add_i32 s78, s78, s40
	s_lshl_b32 s6, s43, 6
	s_sub_i32 s83, s44, s6
	s_lshl_b32 s6, s43, 8
	s_add_i32 s82, s78, s6
	v_add_u32_e32 v208, s82, v172
	v_add_u32_e32 v209, s82, v173
	ds_read_b32 v212, v208 offset:0
	ds_read_b32 v213, v208 offset:32
	ds_read_b32 v214, v208 offset:64
	ds_read_b32 v215, v208 offset:96
	ds_read_b32 v216, v208 offset:128
	ds_read_b32 v217, v208 offset:160
	ds_read_b32 v218, v208 offset:192
	ds_read_b32 v219, v208 offset:224
	ds_read_b32 v198, v209
	s_waitcnt lgkmcnt(0)
	v_mov_b32_e32 v183, v121
	s_mov_b64 s[84:85], -1
	s_mov_b32 s77, 1
	s_branch .Lmk_gather

.LBB2_61:
	s_cmp_lt_i32 s50, 38
	v_mov_b32_e32 v183, v198
	s_cbranch_scc0 .LBB2_116

.LBB2_64:
	s_mov_b64 s[54:55], s[6:7]
	s_lshl_b32 s66, s49, 6
	s_sub_i32 s66, s41, s66
	s_cmp_gt_i32 s66, 32
	s_cselect_b64 s[80:81], -1, 0
	s_add_i32 s11, s45, -1
	s_cmp_eq_u32 s49, s11
	s_cselect_b64 s[84:85], -1, 0
	v_cmp_gt_i32_e64 s[56:57], s66, v110
	s_and_b64 vcc, exec, s[54:55]
	s_cbranch_vccz .Lmk_ua_ready
	s_waitcnt vmcnt(12)
.Lmk_ua_ready:
	s_waitcnt lgkmcnt(8)
	v_mfma_f32_16x16x32_f16 v[200:203], v[240:243], v[208:211], 0
	ds_read_b64_tr_b16 v[146:147], v186 offset:4096
	ds_read_b64_tr_b16 v[148:149], v186 offset:6144
	v_mfma_f32_16x16x32_f16 v[200:203], v[244:247], v[212:215], v[200:203]
	ds_read_b64_tr_b16 v[150:151], v188 offset:4096
	ds_read_b64_tr_b16 v[152:153], v188 offset:6144
	v_mfma_f32_16x16x32_f16 v[160:163], v[240:243], v[216:219], 0
	ds_read_b64_tr_b16 v[154:155], v189 offset:4096
	ds_read_b64_tr_b16 v[156:157], v189 offset:6144
	v_mfma_f32_16x16x32_f16 v[160:163], v[244:247], v[220:223], v[160:163]
	ds_read_b64_tr_b16 v[204:205], v190 offset:4096
	ds_read_b64_tr_b16 v[206:207], v190 offset:6144
	v_mfma_f32_16x16x32_f16 v[248:251], v[240:243], v[224:227], 0
	s_lshl_b32 s6, s43, 6
	s_sub_i32 s83, s44, s6
	s_lshl_b32 s6, s43, 8
	s_add_i32 s82, s78, s6
	v_mfma_f32_16x16x32_f16 v[248:251], v[244:247], v[228:231], v[248:251]
	v_add_u32_e32 v208, s82, v172
	v_add_u32_e32 v209, s82, v173
	ds_read_b32 v212, v208 offset:0
	v_mfma_f32_16x16x32_f16 v[252:255], v[240:243], v[232:235], 0
	ds_read_b32 v213, v208 offset:32
	ds_read_b32 v214, v208 offset:64
	ds_read_b32 v215, v208 offset:96
	v_mfma_f32_16x16x32_f16 v[252:255], v[244:247], v[236:239], v[252:255]
	ds_read_b32 v216, v208 offset:128
	ds_read_b32 v217, v208 offset:160
	ds_read_b32 v218, v208 offset:192
	ds_read_b32 v219, v208 offset:224
	ds_read_b32 v198, v209
	v_mov_b64_e32 v[210:211], s[12:13]
	v_mov_b64_e32 v[208:209], s[12:13]
	s_and_b64 vcc, exec, s[84:85]
	s_cbranch_vccz .Lmk_no_ua
	s_add_i32 s11, s50, 1
	v_lshlrev_b32_e32 v34, 4, v107
	v_lshl_or_b32 v34, s11, 8, v34
	global_load_dwordx4 v[240:243], v34, s[58:59]
	global_load_dwordx4 v[244:247], v34, s[58:59] offset:64
.Lmk_no_ua:
	v_cndmask_b32_e64 v201, v195, v185, s[54:55]
	v_add_f32_e32 v202, 0x40200000, v201
	v_cndmask_b32_e64 v34, v200, v160, s[60:61]
	v_cndmask_b32_e64 v34, v34, v248, s[62:63]
	v_cndmask_b32_e64 v34, v34, v252, s[64:65]
	v_add_f32_e32 v34, v34, v121
	v_mul_f32_e32 v121, 0x3e4ccccd, v34
	v_max_f32_e32 v34, v34, v121
	v_cmp_gt_f32_e32 vcc, v34, v202
	s_and_b64 s[68:69], s[56:57], vcc
	s_cmp_eq_u64 s[68:69], 0
	s_cbranch_scc1 .Lmk_nomax
	v_cndmask_b32_e64 v161, v185, v34, s[56:57]
	s_nop 1
	v_max_f32_dpp v161, v161, v161 row_shr:1 row_mask:0xf bank_mask:0xf
	s_nop 1
	v_max_f32_dpp v161, v161, v161 row_shr:2 row_mask:0xf bank_mask:0xf
	s_nop 1
	v_max_f32_dpp v161, v161, v161 row_shr:4 row_mask:0xf bank_mask:0xf
	s_nop 1
	v_max_f32_dpp v161, v161, v161 row_shr:8 row_mask:0xf bank_mask:0xf
	s_nop 1
	v_max_f32_dpp v161, v161, v161 row_bcast:15 row_mask:0xa bank_mask:0xf
	s_nop 1
	v_max_f32_dpp v161, v161, v161 row_bcast:31 row_mask:0xc bank_mask:0xf
	s_nop 1
	v_readlane_b32 s70, v161, 63
	s_and_b64 vcc, exec, s[54:55]
	s_nop 0
	v_mov_b32_e32 v161, s70
	s_cbranch_vccnz .Lmk_norescale
	v_sub_f32_e32 v162, v195, v161
	v_mul_f32_e32 v162, 0x3fb8aa3b, v162
	v_exp_f32_e32 v248, v162
	s_nop 0
	v_pk_mul_f32 v[56:57], v[248:249], v[56:57] op_sel_hi:[0,1]
	v_pk_mul_f32 v[54:55], v[248:249], v[54:55] op_sel_hi:[0,1]
	v_pk_mul_f32 v[60:61], v[248:249], v[60:61] op_sel_hi:[0,1]
	v_pk_mul_f32 v[58:59], v[248:249], v[58:59] op_sel_hi:[0,1]
	v_pk_mul_f32 v[64:65], v[248:249], v[64:65] op_sel_hi:[0,1]
	v_pk_mul_f32 v[62:63], v[248:249], v[62:63] op_sel_hi:[0,1]
	v_pk_mul_f32 v[68:69], v[248:249], v[68:69] op_sel_hi:[0,1]
	v_pk_mul_f32 v[66:67], v[248:249], v[66:67] op_sel_hi:[0,1]
	v_pk_mul_f32 v[72:73], v[72:73], v[248:249] op_sel_hi:[1,0]
	v_pk_mul_f32 v[70:71], v[70:71], v[248:249] op_sel_hi:[1,0]

.Lmk_nomax:
	v_mov_b32_e32 v195, v201
	v_sub_f32_e32 v34, v34, v195
	v_fmamk_f32 v34, v34, 0x3fb8aa3b, v187
	v_exp_f32_e32 v34, v34
	s_nop 0
	v_cvt_f16_f32_e32 v34, v34
	v_cndmask_b32_e64 v34, 0, v34, s[56:57]
	ds_write_b16 v115, v34
	ds_read_b64_tr_b16 v[200:201], v193 offset:0
	ds_read_b64_tr_b16 v[202:203], v193 offset:512
	ds_read_b64_tr_b16 v[160:161], v193 offset:1024
	ds_read_b64_tr_b16 v[162:163], v193 offset:1536
	s_and_b64 vcc, exec, s[54:55]
	s_cbranch_vccnz .Lmk_w_first
	s_and_b64 vcc, exec, s[84:85]
	s_cbranch_vccnz .Lmk_w2
	s_waitcnt vmcnt(0)
	s_branch .Lmk_wdone
.Lmk_w2:
	s_waitcnt vmcnt(2)
	s_branch .Lmk_wdone
.Lmk_w_first:
	s_and_b64 vcc, exec, s[84:85]
	s_cbranch_vccnz .Lmk_w10
	s_waitcnt vmcnt(8)
	s_branch .Lmk_wdone

.Lmk_wdone:
	ds_write_b16 v115, v35
	ds_write_b128 v196, v[10:13]
	ds_write_b128 v196, v[14:17] offset:1024
	ds_write_b128 v196, v[30:33] offset:2048
	ds_write_b128 v196, v[26:29] offset:3072
	s_and_b64 vcc, exec, s[54:55]
	s_waitcnt lgkmcnt(5)
	s_cbranch_vccnz .Lmk_agg_first
	v_mfma_f32_16x16x32_f16 v[54:57], v[130:133], v[200:203], v[54:57]
	v_mfma_f32_16x16x32_f16 v[58:61], v[134:137], v[200:203], v[58:61]
	v_mfma_f32_16x16x32_f16 v[62:65], v[138:141], v[200:203], v[62:65]
	v_mfma_f32_16x16x32_f16 v[66:69], v[142:145], v[200:203], v[66:69]
	v_mfma_f32_16x16x32_f16 v[70:73], v[208:211], v[200:203], v[70:73]
	s_branch .Lmk_agg_join
.Lmk_agg_first:
	v_mfma_f32_16x16x32_f16 v[54:57], v[130:133], v[200:203], 0
	v_mfma_f32_16x16x32_f16 v[58:61], v[134:137], v[200:203], 0
	v_mfma_f32_16x16x32_f16 v[62:65], v[138:141], v[200:203], 0
	v_mfma_f32_16x16x32_f16 v[66:69], v[142:145], v[200:203], 0
	v_mfma_f32_16x16x32_f16 v[70:73], v[208:211], v[200:203], 0

.LBB2_76:
	s_and_b64 vcc, exec, s[0:1]
	s_cbranch_vccnz .LBB2_110
	s_cmp_gt_i32 s50, 35
	s_cbranch_scc1 .LBB2_110
	s_add_i32 s36, s50, 2
	s_mul_hi_i32 s0, s36, 0x55555556
	s_lshr_b32 s1, s0, 31
	s_add_i32 s0, s0, s1
	s_mul_i32 s0, s0, 3
	s_sub_i32 s37, s36, s0
	s_mulk_i32 s37, 0xc00
	s_add_i32 s38, s40, s37
	v_readlane_b32 s10, v111, s36
	s_nop 1
	v_add_u32_e32 v36, s10, v110
	v_cmp_gt_u32_e32 vcc, s48, v36
	v_lshl_add_u32 v36, v36, 2, s38
	s_and_saveexec_b64 s[0:1], vcc
	ds_write_b32 v36, v35
	s_or_b64 exec, exec, s[0:1]
	s_and_saveexec_b64 s[0:1], s[4:5]
	v_lshl_add_u32 v36, v110, 2, s38
	ds_write_b32 v36, v194
	s_or_b64 exec, exec, s[0:1]
	v_add_u32_e32 v36, v129, v165
	v_cmp_lt_i32_e32 vcc, v114, v169
	v_cmp_gt_i32_e64 s[0:1], s48, v36
	v_add_u32_e32 v36, v129, v114
	s_and_b64 s[52:53], vcc, s[0:1]
	v_lshl_add_u32 v37, v36, 2, s38
	s_waitcnt vmcnt(8)
	s_and_saveexec_b64 s[0:1], s[52:53]
	ds_write_b32 v37, v125 offset:64
	s_or_b64 exec, exec, s[0:1]
	v_add_u32_e32 v121, v129, v166
	v_cmp_lt_i32_e32 vcc, v109, v169
	v_cmp_gt_i32_e64 s[0:1], s48, v121
	s_and_b64 s[38:39], vcc, s[0:1]
	s_and_saveexec_b64 s[0:1], s[38:39]
	ds_write_b32 v37, v117 offset:80
	s_or_b64 exec, exec, s[0:1]
	v_add_u32_e32 v121, v129, v167
	v_cmp_lt_i32_e32 vcc, v123, v169
	v_cmp_gt_i32_e64 s[0:1], s48, v121
	s_and_b64 s[38:39], vcc, s[0:1]
	s_and_saveexec_b64 s[0:1], s[38:39]
	ds_write_b32 v37, v171 offset:96
	s_or_b64 exec, exec, s[0:1]
	v_add_u32_e32 v121, v129, v168
	v_cmp_lt_i32_e32 vcc, v164, v169
	v_cmp_gt_i32_e64 s[0:1], s48, v121
	s_and_b64 s[38:39], vcc, s[0:1]
	s_and_saveexec_b64 s[0:1], s[38:39]
	ds_write_b32 v37, v170 offset:112
	s_or_b64 exec, exec, s[0:1]
	v_cmp_lt_i32_e32 vcc, v165, v169
	s_and_saveexec_b64 s[0:1], vcc
	s_cbranch_execz .LBB2_109
	v_ashrrev_i32_e32 v121, 31, v120
	s_add_i32 s37, s47, s37
	v_lshl_add_u32 v130, v36, 2, s37
	v_lshlrev_b64 v[36:37], 2, v[120:121]
	v_mad_i64_i32 v[36:37], s[36:37], s36, v116, v[36:37]
	v_lshl_add_u64 v[36:37], v[0:1], 0, v[36:37]
	s_mov_b64 s[36:37], 0
	v_mov_b32_e32 v121, v165
	s_branch .LBB2_91

.LBB2_110:
	s_add_i32 s11, s50, 2
	s_cmp_eq_u32 s42, s11
	s_cbranch_scc0 .Lmk_gather
	s_and_b64 vcc, exec, s[54:55]
	s_cbranch_vccz .Lmk_gather
	s_lshl_b32 s6, s43, 6
	s_sub_i32 s83, s44, s6
	s_lshl_b32 s6, s43, 8
	s_add_i32 s82, s78, s6
	v_add_u32_e32 v208, s82, v172
	v_add_u32_e32 v209, s82, v173
	ds_read_b32 v212, v208 offset:0
	ds_read_b32 v213, v208 offset:32
	ds_read_b32 v214, v208 offset:64
	ds_read_b32 v215, v208 offset:96
	ds_read_b32 v216, v208 offset:128
	ds_read_b32 v217, v208 offset:160
	ds_read_b32 v218, v208 offset:192
	ds_read_b32 v219, v208 offset:224
	ds_read_b32 v198, v209
	s_waitcnt lgkmcnt(0)
.Lmk_gather:
	v_and_b32_e32 v10, 0xffff, v212
	v_and_b32_e32 v14, 0xffff, v213
	v_and_b32_e32 v30, 0xffff, v214
	v_and_b32_e32 v26, 0xffff, v215
	s_cmp_gt_i32 s83, 32
	v_lshl_or_b32 v10, v10, 7, v176
	v_lshl_or_b32 v14, v14, 7, v176
	s_cselect_b64 s[30:31], -1, 0
	v_lshl_or_b32 v30, v30, 7, v176
	v_lshl_or_b32 v26, v26, 7, v176
	s_cmp_lt_i32 s83, 33
	global_load_dwordx4 v[10:13], v10, s[28:29]
	global_load_dwordx4 v[14:17], v14, s[28:29]
	global_load_dwordx4 v[30:33], v30, s[28:29]
	global_load_dwordx4 v[26:29], v26, s[28:29]
	s_cbranch_scc1 .LBB2_68
	v_and_b32_e32 v2, 0xffff, v216
	v_and_b32_e32 v6, 0xffff, v217
	v_and_b32_e32 v18, 0xffff, v218
	v_and_b32_e32 v22, 0xffff, v219
	v_lshl_or_b32 v2, v2, 7, v176
	v_lshl_or_b32 v6, v6, 7, v176
	v_lshl_or_b32 v18, v18, 7, v176
	v_lshl_or_b32 v22, v22, 7, v176
	global_load_dwordx4 v[2:5], v2, s[28:29]
	global_load_dwordx4 v[6:9], v6, s[28:29]
	global_load_dwordx4 v[18:21], v18, s[28:29]
	global_load_dwordx4 v[22:25], v22, s[28:29]

.LBB2_72:
	v_bfe_u32 v34, v183, 16, 4
	v_cndmask_b32_e64 v121, v197, v184, s[84:85]
	v_lshl_add_u32 v115, v34, 1, v191
	v_lshlrev_b32_e32 v34, 2, v34
	ds_bpermute_b32 v121, v34, v121
	v_xor_b32_e32 v34, 64, v122
	ds_read_b128 v[208:211], v122
	ds_read_b128 v[212:215], v34
	ds_read_b128 v[216:219], v122 offset:2048
	ds_read_b128 v[220:223], v34 offset:2048
	ds_read_b128 v[224:227], v122 offset:4096
	ds_read_b128 v[228:231], v34 offset:4096
	ds_read_b128 v[232:235], v122 offset:6144
	ds_read_b128 v[236:239], v34 offset:6144
	ds_read_b64_tr_b16 v[130:131], v186 offset:0
	ds_read_b64_tr_b16 v[132:133], v186 offset:2048
	ds_read_b64_tr_b16 v[134:135], v188 offset:0
	ds_read_b64_tr_b16 v[136:137], v188 offset:2048
	ds_read_b64_tr_b16 v[138:139], v189 offset:0
	ds_read_b64_tr_b16 v[140:141], v189 offset:2048
	ds_read_b64_tr_b16 v[142:143], v190 offset:0
	ds_read_b64_tr_b16 v[144:145], v190 offset:2048
	s_cmp_lg_u32 s77, 0
	s_cbranch_scc1 .Lmk_primed

.Lmk_ma_ready:
	s_nop 0
	v_div_scale_f32 v36, s[36:37], v70, v70, 1.0
	v_rcp_f32_e32 v37, v36
	v_div_scale_f32 v34, vcc, 1.0, v70, 1.0
	v_mov_b32_e32 v250, v59
	v_fma_f32 v248, -v36, v37, 1.0
	v_fmac_f32_e32 v37, v248, v37
	v_mul_f32_e32 v248, v34, v37
	v_fma_f32 v249, -v36, v248, v34
	v_fmac_f32_e32 v248, v249, v37
	v_fma_f32 v36, -v36, v248, v34
	v_div_fmas_f32 v36, v36, v37, v248
	v_div_fixup_f32 v36, v36, v70, 1.0
	v_fma_mixlo_f16 v37, v36, v54, 0
	v_mov_b32_e32 v248, v55
	v_mov_b32_e32 v249, v56
	v_pk_mul_f32 v[248:249], v[36:37], v[248:249] op_sel_hi:[0,1]
	v_mov_b32_e32 v251, v60
	v_cvt_pk_f16_f32 v249, v248, v249
	v_pk_mul_f32 v[250:251], v[36:37], v[250:251] op_sel_hi:[0,1]
	v_pack_b32_f16 v248, v37, v249
	v_cvt_pk_f16_f32 v37, v250, v251
	v_mov_b32_e32 v250, v63
	v_mov_b32_e32 v251, v64
	v_pk_mul_f32 v[250:251], v[36:37], v[250:251] op_sel_hi:[0,1]
	v_cvt_pk_f16_f32 v253, v250, v251
	v_mov_b32_e32 v250, v67
	v_mov_b32_e32 v251, v68
	v_fma_mixlo_f16 v34, v36, v62, 0
	v_pk_mul_f32 v[250:251], v[36:37], v[250:251] op_sel_hi:[0,1]
	v_pack_b32_f16 v252, v34, v253
	v_cvt_pk_f16_f32 v34, v250, v251
	v_pk_mov_b32 v[250:251], v[56:57], v[58:59] op_sel:[1,0]
	v_pk_mov_b32 v[254:255], v[64:65], v[66:67] op_sel:[1,0]
	v_pk_mul_f32 v[250:251], v[36:37], v[250:251] op_sel_hi:[0,1]
	v_cvt_pk_f16_f32 v250, v250, v251
	v_lshrrev_b32_e32 v251, 16, v37
	v_pk_mul_f32 v[254:255], v[36:37], v[254:255] op_sel_hi:[0,1]
	v_alignbit_b32 v249, v250, v249, 16
	v_alignbit_b32 v250, v37, v250, 16
	v_fma_mixhi_f16 v251, v36, v61, 0
	v_cvt_pk_f16_f32 v37, v254, v255
	v_lshrrev_b32_e32 v255, 16, v34
	v_alignbit_b32 v253, v37, v253, 16
	v_mfma_f32_16x16x32_f16 v[50:53], v[86:89], v[248:251], v[50:53]
	v_alignbit_b32 v254, v34, v37, 16
	v_fma_mixhi_f16 v255, v36, v69, 0
	v_mfma_f32_16x16x32_f16 v[46:49], v[78:81], v[248:251], v[46:49]
	v_mfma_f32_16x16x32_f16 v[42:45], v[90:93], v[248:251], v[42:45]
	v_mfma_f32_16x16x32_f16 v[36:39], v[98:101], v[248:251], v[38:41]
	v_mfma_f32_16x16x32_f16 v[50:53], v[82:85], v[252:255], v[50:53]
	v_mfma_f32_16x16x32_f16 v[46:49], v[74:77], v[252:255], v[46:49]
	v_mfma_f32_16x16x32_f16 v[42:45], v[94:97], v[252:255], v[42:45]
	v_mfma_f32_16x16x32_f16 v[38:41], v[102:105], v[252:255], v[36:39]

.LBB2_93:
	s_cmp_gt_i32 s50, 35
	v_mov_b32_e32 v169, 0
	s_cbranch_scc1 .LBB2_103
	v_sub_u32_e32 v169, v174, v124
	v_cndmask_b32_e64 v34, 0, v169, s[2:3]
	s_add_i32 s0, s50, 2
	v_mov_b32_e32 v74, 0
	v_add_u32_dpp v34, v34, v34 row_shr:1 row_mask:0xf bank_mask:0xf bound_ctrl:1
	v_mad_i64_i32 v[36:37], s[0:1], s0, v116, v[118:119]
	s_nop 0
	v_add_u32_dpp v34, v34, v34 row_shr:2 row_mask:0xf bank_mask:0xf bound_ctrl:1
	v_ashrrev_i32_e32 v125, 31, v124
	v_mov_b32_e32 v117, 0
	v_add_u32_dpp v34, v34, v34 row_shr:4 row_mask:0xf bank_mask:0xf bound_ctrl:1
	v_lshl_add_u64 v[36:37], v[124:125], 2, v[36:37]
	v_cmp_lt_i32_e32 vcc, v114, v169
	v_add_u32_dpp v34, v34, v34 row_shr:8 row_mask:0xf bank_mask:0xf bound_ctrl:1
	v_mov_b32_e32 v125, 0
	s_nop 0
	v_add_u32_dpp v34, v34, v34 row_bcast:15 row_mask:0xa bank_mask:0xf
	s_nop 1
	v_mov_b32_dpp v74, v34 row_bcast:31 row_mask:0xc bank_mask:0xf
	s_and_saveexec_b64 s[0:1], vcc
	s_cbranch_execz .LBB2_96
	v_mov_b32_e32 v129, v35
	v_lshl_add_u64 v[76:77], v[36:37], 0, v[128:129]
	global_load_dword v125, v[76:77], off
